# E6 with per-MMA-block s_setprio toggles removed and one static s_setprio 1 for the staggered wave half (wr==1) per GEMM phase
# baseline (speedup 1.0000x reference)
.LBB0_249:
	s_cmp_gt_i32 s34, 2
	s_cselect_b64 s[2:3], -1, 0
	s_cmp_lt_i32 s35, 3
	s_cselect_b64 s[4:5], -1, 0
	s_or_b64 s[2:3], s[2:3], s[4:5]
	s_and_b64 vcc, exec, s[2:3]
	s_cbranch_vccnz .LBB0_336
	s_mov_b32 s2, 24
	s_lshl_b32 s2, s2, 3
	s_add_i32 s2, s2, 0
	s_add_i32 s2, s2, 0x201c0
	v_mov_b32_e32 v0, s2
	ds_read_b32 v1, v0
	ds_read_b32 v0, v0 offset:4
	s_load_dword s42, s[0:1], 0xd0
	s_add_u32 s4, s0, 0xd0
	s_addc_u32 s5, s1, 0
	s_mov_b32 s45, s10
	s_and_b32 s43, s33, 0xffffffc0
	s_waitcnt lgkmcnt(0)
	s_mov_b32 s44, s42
	v_readfirstlane_b32 s15, v0
	v_mbcnt_lo_u32_b32 v9, -1, 0
	v_mbcnt_hi_u32_b32 v9, -1, v9
	v_readfirstlane_b32 s14, v1
	v_add_u32_e32 v0, s43, v9
	s_cmpk_gt_i32 s45, 0x5ff
	v_readfirstlane_b32 s3, v0
	s_cbranch_scc1 .LBB0_270
	s_add_u32 s46, s14, 0x26000000
	s_addc_u32 s47, s15, 0
	v_lshlrev_b32_e32 v8, 4, v0
	v_lshrrev_b32_e32 v1, 5, v0
	v_lshrrev_b32_e32 v3, 1, v0
	s_add_u32 s48, s14, 0x200000
	v_and_b32_e32 v1, 4, v1
	v_bfe_u32 v2, v8, 6, 2
	v_and_b32_e32 v3, 24, v3
	v_add_u32_e32 v12, 0x2000, v8
	s_addc_u32 s49, s15, 0
	v_or3_b32 v1, v1, v2, v3
	v_lshrrev_b32_e32 v2, 7, v12
	s_mov_b32 s2, 0x1fffe0
	v_and_b32_e32 v11, 64, v0
	v_bfe_u32 v0, v0, 3, 25
	s_ashr_i32 s51, s45, 31
	v_and_or_b32 v3, v2, s2, v1
	v_and_or_b32 v1, v0, s2, v1
	s_lshr_b32 s2, s51, 29
	v_bfe_u32 v13, v8, 6, 4
	s_mov_b32 s6, 0x1ffff0
	s_add_i32 s2, s45, s2
	s_ashr_i32 s16, s3, 6
	v_and_or_b32 v2, v2, s6, v13
	v_and_or_b32 v0, v0, s6, v13
	s_ashr_i32 s6, s2, 3
	s_and_b32 s2, s2, -8
	s_ashr_i32 s18, s3, 8
	s_lshl_b32 s50, s16, 10
	s_sub_i32 s2, s45, s2
	s_cmp_lt_i32 s2, 0
	s_movk_i32 s52, 0xc1
	s_cselect_b32 s7, s52, 0xc0
	s_mul_i32 s2, s7, s2
	s_add_i32 s2, s2, s6
	s_mul_hi_i32 s6, s2, 0x2aaaaaab
	s_lshr_b32 s7, s6, 31
	s_ashr_i32 s6, s6, 4
	s_add_i32 s6, s6, s7
	s_lshl_b32 s7, s6, 3
	s_mulk_i32 s6, 0x60
	s_sub_i32 s6, s2, s6
	s_bfe_i32 s2, s6, 0x80000
	s_bfe_u32 s2, s2, 0x3000c
	s_add_i32 s8, s6, s2
	s_bfe_i32 s2, s8, 0x80000
	s_and_b32 s8, s8, 0xf8
	s_sub_i32 s6, s6, s8
	s_sext_i32_i8 s6, s6
	s_add_i32 s28, s7, s6
	s_sext_i32_i16 s2, s2
	s_ashr_i32 s29, s28, 31
	s_lshr_b32 s2, s2, 3
	s_lshl_b64 s[6:7], s[28:29], 19
	s_add_u32 s30, s46, s6
	s_addc_u32 s31, s47, s7
	s_bfe_i64 s[6:7], s[2:3], 0x100000
	v_and_b32_e32 v4, 32, v9
	s_lshl_b64 s[6:7], s[6:7], 19
	v_bitop3_b32 v10, v8, v4, 48 bitop3:0x6c
	s_add_u32 s36, s48, s6
	v_or_b32_e32 v4, v10, v11
	s_addc_u32 s37, s49, s7
	s_add_i32 s53, s50, 0
	v_lshl_or_b32 v132, v1, 11, v4
	s_add_i32 m0, s53, 0x10000
	v_lshl_or_b32 v128, v3, 11, v4
	global_load_lds_dwordx4 v132, s[36:37]
	s_add_i32 m0, s53, 0x12000
	s_add_u32 s6, s36, 0x40000
	global_load_lds_dwordx4 v128, s[36:37]
	s_addc_u32 s7, s37, 0
	s_add_i32 m0, s53, 0x14000
	s_add_i32 s54, s53, 0x2000
	global_load_lds_dwordx4 v132, s[6:7]
	s_add_i32 m0, s53, 0x16000
	v_lshl_or_b32 v134, v0, 11, v4
	global_load_lds_dwordx4 v128, s[6:7]
	s_mov_b32 m0, s53
	s_add_u32 s6, s30, 0x40000
	v_lshl_or_b32 v130, v2, 11, v4
	global_load_lds_dwordx4 v134, s[30:31]
	s_mov_b32 m0, s54
	s_addc_u32 s7, s31, 0
	s_add_i32 s55, s53, 0x4000
	global_load_lds_dwordx4 v130, s[30:31]
	s_mov_b32 m0, s55
	s_add_i32 s56, s53, 0x6000
	global_load_lds_dwordx4 v134, s[6:7]
	s_mov_b32 m0, s56
	v_mov_b32_e32 v137, 0
	global_load_lds_dwordx4 v130, s[6:7]
	v_mov_b32_e32 v133, v137
	v_mov_b32_e32 v129, v137
	v_mov_b32_e32 v135, v137
	v_mov_b32_e32 v131, v137
	s_cmp_eq_u32 s18, 1
	v_lshl_add_u64 v[6:7], s[36:37], 0, v[132:133]
	v_lshl_add_u64 v[4:5], s[36:37], 0, v[128:129]
	v_lshl_add_u64 v[0:1], s[30:31], 0, v[134:135]
	s_cselect_b64 s[6:7], -1, 0
	s_setprio 0
	s_cmp_lg_u32 s18, 1
	v_lshl_add_u64 v[2:3], s[30:31], 0, v[130:131]
	s_cbranch_scc1 .LBB0_253
	s_setprio 1
	s_barrier

.LBB0_418:
	v_lshlrev_b32_e32 v10, 4, v0
	v_and_b32_e32 v1, 32, v9
	v_bitop3_b32 v11, v10, v1, 48 bitop3:0x6c
	v_lshrrev_b32_e32 v1, 1, v0
	v_lshrrev_b32_e32 v2, 5, v0
	s_ashr_i32 s3, s20, 6
	v_and_b32_e32 v1, 24, v1
	v_and_b32_e32 v2, 4, v2
	v_bfe_u32 v3, v10, 6, 2
	v_bfe_u32 v13, v10, 6, 4
	v_or3_b32 v1, v2, v3, v1
	v_and_b32_e32 v12, 64, v0
	v_bfe_u32 v0, v0, 3, 25
	s_mov_b32 s2, 0x1ffff0
	s_mov_b32 s4, 0x1fffe0
	s_lshl_b32 s50, s3, 10
	v_or_b32_e32 v2, v11, v12
	v_and_or_b32 v3, v0, s2, v13
	v_and_or_b32 v0, v0, s4, v1
	v_add_u32_e32 v14, 0x2000, v10
	s_add_i32 s51, s50, 0
	v_lshl_or_b32 v194, v0, 11, v2
	v_lshrrev_b32_e32 v0, 7, v14
	s_add_i32 m0, s51, 0x10000
	v_lshl_or_b32 v192, v3, 11, v2
	v_and_or_b32 v3, v0, s2, v13
	v_and_or_b32 v0, v0, s4, v1
	s_ashr_i32 s2, s20, 8
	global_load_lds_dwordx4 v194, s[36:37]
	s_add_i32 m0, s51, 0x12000
	v_lshl_or_b32 v198, v0, 11, v2
	s_add_u32 s4, s36, 0x40000
	global_load_lds_dwordx4 v198, s[36:37]
	s_addc_u32 s5, s37, 0
	s_add_i32 m0, s51, 0x14000
	s_add_i32 s52, s51, 0x2000
	global_load_lds_dwordx4 v194, s[4:5]
	s_add_i32 m0, s51, 0x16000
	v_lshl_or_b32 v196, v3, 11, v2
	global_load_lds_dwordx4 v198, s[4:5]
	s_mov_b32 m0, s51
	s_add_u32 s4, s30, 0x40000
	global_load_lds_dwordx4 v192, s[30:31]
	s_mov_b32 m0, s52
	s_addc_u32 s5, s31, 0
	s_add_i32 s53, s51, 0x4000
	global_load_lds_dwordx4 v196, s[30:31]
	s_mov_b32 m0, s53
	s_add_i32 s54, s51, 0x6000
	global_load_lds_dwordx4 v192, s[4:5]
	s_mov_b32 m0, s54
	v_mov_b32_e32 v195, 0
	global_load_lds_dwordx4 v196, s[4:5]
	v_mov_b32_e32 v199, v195
	v_mov_b32_e32 v193, v195
	v_mov_b32_e32 v197, v195
	s_cmp_eq_u32 s2, 1
	s_mov_b32 s9, 0
	v_lshl_add_u64 v[6:7], s[36:37], 0, v[194:195]
	v_lshl_add_u64 v[4:5], s[36:37], 0, v[198:199]
	v_lshl_add_u64 v[0:1], s[30:31], 0, v[192:193]
	s_cselect_b64 s[12:13], -1, 0
	s_setprio 0
	s_cmp_lg_u32 s2, 1
	v_lshl_add_u64 v[2:3], s[30:31], 0, v[196:197]
	s_cbranch_scc1 .LBB0_420
	s_setprio 1
	s_barrier

.LBB0_533:
	v_lshlrev_b32_e32 v4, 4, v80
	v_and_b32_e32 v0, 32, v8
	v_bfe_u32 v7, v80, 2, 4
	v_bitop3_b32 v5, v4, v0, 48 bitop3:0x6c
	v_and_b32_e32 v6, 64, v80
	v_lshrrev_b32_e32 v1, 3, v80
	s_mov_b32 s3, 0x1ffff0
	v_or_b32_e32 v0, v5, v6
	v_and_or_b32 v1, v1, s3, v7
	v_add_u32_e32 v9, 0x2000, v4
	s_ashr_i32 s2, s4, 6
	v_lshl_or_b32 v64, v1, 11, v0
	v_lshrrev_b32_e32 v1, 7, v9
	v_and_or_b32 v1, v1, s3, v7
	s_ashr_i32 s3, s4, 8
	s_lshl_b32 s50, s2, 10
	s_add_u32 s51, s30, 0x26000000
	s_addc_u32 s52, s31, 0
	s_add_u32 s12, s30, 0x1e00000
	s_addc_u32 s13, s31, 0
	s_add_i32 s8, s5, s8
	s_ashr_i32 s9, s8, 31
	s_lshl_b64 s[14:15], s[8:9], 19
	s_add_u32 s22, s51, s14
	s_addc_u32 s23, s52, s15
	s_add_i32 s9, s50, 0
	s_add_i32 m0, s9, 0x10000
	v_lshl_or_b32 v66, v1, 11, v0
	global_load_lds_dwordx4 v64, s[12:13]
	s_add_i32 m0, s9, 0x12000
	s_add_u32 s14, s30, 0x1e40000
	s_addc_u32 s15, s31, 0
	s_add_i32 s53, s9, 0x14000
	global_load_lds_dwordx4 v66, s[12:13]
	s_mov_b32 m0, s53
	s_add_i32 s54, s9, 0x16000
	global_load_lds_dwordx4 v64, s[14:15]
	s_mov_b32 m0, s54
	s_add_i32 s56, s9, 0x2000
	global_load_lds_dwordx4 v66, s[14:15]
	s_mov_b32 m0, s9
	s_add_u32 s14, s22, 0x40000
	global_load_lds_dwordx4 v64, s[22:23]
	s_mov_b32 m0, s56
	s_addc_u32 s15, s23, 0
	s_add_i32 s57, s9, 0x4000
	global_load_lds_dwordx4 v66, s[22:23]
	s_mov_b32 m0, s57
	s_add_i32 s58, s9, 0x6000
	global_load_lds_dwordx4 v64, s[14:15]
	s_mov_b32 m0, s58
	v_mov_b32_e32 v65, 0
	global_load_lds_dwordx4 v66, s[14:15]
	v_mov_b32_e32 v67, v65
	s_cmp_eq_u32 s3, 1
	s_mov_b32 s64, 0
	v_lshl_add_u64 v[0:1], s[22:23], 0, v[64:65]
	s_cselect_b64 s[14:15], -1, 0
	s_setprio 0
	s_cmp_lg_u32 s3, 1
	v_lshl_add_u64 v[2:3], s[22:23], 0, v[66:67]
	s_cbranch_scc1 .LBB0_535
	s_setprio 1
	s_barrier

.LBB0_773:
	s_or_b64 exec, exec, s[12:13]
	v_and_b32_e32 v10, 32, v8
	v_bitop3_b32 v10, v2, v10, 48 bitop3:0x6c
	v_and_or_b32 v150, v0, 64, v10
	v_lshlrev_b32_e32 v0, 1, v9
	v_lshrrev_b32_e32 v2, 9, v2
	v_or_b32_e32 v138, v3, v150
	v_and_b32_e32 v0, 24, v0
	v_and_b32_e32 v2, 4, v2
	v_and_b32_e32 v3, 3, v9
	s_ashr_i32 s18, s20, 6
	v_or3_b32 v0, v2, v3, v0
	s_mov_b32 s12, 0x1fffe0
	s_lshl_b32 s29, s18, 10
	v_and_or_b32 v1, v1, s12, v0
	s_add_i32 s50, s29, 0
	v_lshl_or_b32 v128, v1, 11, v150
	s_add_i32 m0, s50, 0x10000
	s_ashr_i32 s21, s20, 8
	v_and_or_b32 v0, v5, s12, v0
	global_load_lds_dwordx4 v128, s[36:37]
	s_add_i32 m0, s50, 0x12000
	v_lshl_or_b32 v130, v0, 11, v150
	s_add_u32 s12, s36, 0x40000
	global_load_lds_dwordx4 v130, s[36:37]
	s_addc_u32 s13, s37, 0
	s_add_i32 m0, s50, 0x14000
	s_add_i32 s51, s50, 0x2000
	global_load_lds_dwordx4 v128, s[12:13]
	s_add_i32 m0, s50, 0x16000
	v_or_b32_e32 v136, v4, v150
	global_load_lds_dwordx4 v130, s[12:13]
	s_mov_b32 m0, s50
	s_add_i32 s52, s50, 0x4000
	global_load_lds_dwordx4 v138, s[30:31]
	s_mov_b32 m0, s51
	v_or_b32_e32 v134, v7, v150
	global_load_lds_dwordx4 v136, s[30:31]
	s_mov_b32 m0, s52
	s_add_i32 s53, s50, 0x6000
	v_or_b32_e32 v140, v6, v150
	global_load_lds_dwordx4 v134, s[30:31]
	s_mov_b32 m0, s53
	v_mov_b32_e32 v133, 0
	global_load_lds_dwordx4 v140, s[30:31]
	v_mov_b32_e32 v129, v133
	v_mov_b32_e32 v131, v133
	v_mov_b32_e32 v139, v133
	v_mov_b32_e32 v137, v133
	s_cmp_eq_u32 s21, 1
	s_mov_b32 s54, 0
	v_lshl_add_u64 v[6:7], s[36:37], 0, v[128:129]
	v_lshl_add_u64 v[4:5], s[36:37], 0, v[130:131]
	v_lshl_add_u64 v[0:1], s[30:31], 0, v[138:139]
	s_cselect_b64 s[12:13], -1, 0
	s_setprio 0
	s_cmp_lg_u32 s21, 1
	v_lshl_add_u64 v[2:3], s[30:31], 0, v[136:137]
	s_cbranch_scc1 .LBB0_775
	s_setprio 1
	s_barrier

.LBB0_1061:
	v_lshlrev_b32_e32 v1, 4, v0
	v_and_b32_e32 v2, 32, v8
	v_bitop3_b32 v2, v1, v2, 48 bitop3:0x6c
	v_lshrrev_b32_e32 v5, 1, v0
	v_lshrrev_b32_e32 v2, 1, v2
	v_bfe_u32 v3, v0, 2, 26
	v_bfe_u32 v4, v1, 6, 4
	v_and_or_b32 v2, v5, 32, v2
	v_and_b32_e32 v5, 48, v0
	v_lshrrev_b32_e32 v6, 5, v0
	v_lshrrev_b32_e32 v0, 3, v0
	s_mov_b32 s4, 0x1fffff0
	v_and_b32_e32 v6, 4, v6
	v_bfe_u32 v7, v1, 6, 2
	v_and_or_b32 v0, v0, s4, v4
	s_movk_i32 s6, 0x180
	v_or3_b32 v5, v7, v6, v5
	s_movk_i32 s5, 0xc0
	v_mul_lo_u32 v0, v0, s6
	v_and_or_b32 v3, v3, s5, v5
	v_or_b32_e32 v0, v0, v2
	v_lshlrev_b32_e32 v128, 1, v0
	v_mul_u32_u24_e32 v0, 0x180, v3
	v_or_b32_e32 v0, v0, v2
	s_ashr_i32 s14, s16, 6
	v_lshlrev_b32_e32 v130, 1, v0
	v_add_u32_e32 v0, 0x2000, v1
	v_lshrrev_b32_e32 v1, 7, v0
	v_lshrrev_b32_e32 v0, 6, v0
	s_lshl_b32 s46, s14, 10
	v_and_or_b32 v0, v0, s5, v5
	s_add_i32 s47, s46, 0
	v_mul_u32_u24_e32 v0, 0x180, v0
	s_add_i32 m0, s47, 0x10000
	v_or_b32_e32 v0, v0, v2
	s_ashr_i32 s17, s16, 8
	global_load_lds_dwordx4 v130, s[38:39]
	s_add_i32 m0, s47, 0x12000
	v_and_or_b32 v1, v1, s4, v4
	v_lshlrev_b32_e32 v134, 1, v0
	s_add_u32 s4, s38, 0x1800
	global_load_lds_dwordx4 v134, s[38:39]
	s_addc_u32 s5, s39, 0
	s_add_i32 m0, s47, 0x14000
	v_mul_lo_u32 v1, v1, s6
	global_load_lds_dwordx4 v130, s[4:5]
	s_add_i32 m0, s47, 0x16000
	s_add_i32 s48, s47, 0x2000
	v_or_b32_e32 v1, v1, v2
	global_load_lds_dwordx4 v134, s[4:5]
	s_mov_b32 m0, s47
	s_add_u32 s4, s36, 0x18000
	v_lshlrev_b32_e32 v132, 1, v1
	global_load_lds_dwordx4 v128, s[36:37]
	s_mov_b32 m0, s48
	s_addc_u32 s5, s37, 0
	s_add_i32 s50, s47, 0x4000
	global_load_lds_dwordx4 v132, s[36:37]
	s_mov_b32 m0, s50
	s_add_i32 s51, s47, 0x6000
	global_load_lds_dwordx4 v128, s[4:5]
	s_mov_b32 m0, s51
	v_mov_b32_e32 v131, 0
	global_load_lds_dwordx4 v132, s[4:5]
	v_mov_b32_e32 v135, v131
	v_mov_b32_e32 v129, v131
	v_mov_b32_e32 v133, v131
	s_cmp_eq_u32 s17, 1
	v_lshl_add_u64 v[6:7], s[38:39], 0, v[130:131]
	v_lshl_add_u64 v[4:5], s[38:39], 0, v[134:135]
	v_lshl_add_u64 v[0:1], s[36:37], 0, v[128:129]
	s_cselect_b64 s[4:5], -1, 0
	s_setprio 0
	s_cmp_lg_u32 s17, 1
	v_lshl_add_u64 v[2:3], s[36:37], 0, v[132:133]
	s_cbranch_scc1 .LBB0_1063
	s_setprio 1
	s_barrier

.LBB0_1233:
	s_cmp_gt_i32 s34, 14
	s_cselect_b64 s[2:3], -1, 0
	s_cmp_lt_i32 s35, 15
	s_cselect_b64 s[4:5], -1, 0
	s_or_b64 s[2:3], s[2:3], s[4:5]
	s_and_b64 vcc, exec, s[2:3]
	s_cbranch_vccnz .LBB0_1395
	s_mov_b32 s2, 24
	s_lshl_b32 s2, s2, 3
	s_add_i32 s2, s2, 0
	s_add_i32 s2, s2, 0x201c0
	v_mov_b32_e32 v0, s2
	s_waitcnt vmcnt(0) lgkmcnt(0)
	ds_read_b32 v1, v0
	ds_read_b32 v0, v0 offset:4
	s_load_dword s40, s[0:1], 0xd0
	s_add_u32 s4, s0, 0xd0
	s_addc_u32 s5, s1, 0
	s_mov_b32 s43, s10
	s_and_b32 s41, s33, 0xffffffc0
	s_waitcnt lgkmcnt(0)
	s_mov_b32 s42, s40
	v_readfirstlane_b32 s13, v0
	v_mbcnt_lo_u32_b32 v9, -1, 0
	v_mbcnt_hi_u32_b32 v9, -1, v9
	v_readfirstlane_b32 s12, v1
	v_add_u32_e32 v0, s41, v9
	s_cmpk_gt_i32 s43, 0x17f
	v_readfirstlane_b32 s3, v0
	s_cbranch_scc1 .LBB0_1250
	s_add_u32 s44, s12, 0x26000000
	s_addc_u32 s45, s13, 0
	v_lshlrev_b32_e32 v8, 4, v0
	v_lshrrev_b32_e32 v1, 5, v0
	v_lshrrev_b32_e32 v3, 1, v0
	s_add_u32 s46, s12, 0x1200000
	v_and_b32_e32 v1, 4, v1
	v_bfe_u32 v2, v8, 6, 2
	v_and_b32_e32 v3, 24, v3
	v_add_u32_e32 v12, 0x2000, v8
	s_addc_u32 s47, s13, 0
	v_or3_b32 v1, v1, v2, v3
	v_lshrrev_b32_e32 v2, 7, v12
	s_mov_b32 s2, 0x1fffe0
	v_and_b32_e32 v11, 64, v0
	v_bfe_u32 v0, v0, 3, 25
	s_ashr_i32 s49, s43, 31
	v_and_or_b32 v3, v2, s2, v1
	v_and_or_b32 v1, v0, s2, v1
	s_lshr_b32 s2, s49, 29
	v_bfe_u32 v13, v8, 6, 4
	s_mov_b32 s6, 0x1ffff0
	s_add_i32 s2, s43, s2
	s_ashr_i32 s14, s3, 6
	v_and_or_b32 v2, v2, s6, v13
	v_and_or_b32 v0, v0, s6, v13
	s_ashr_i32 s6, s2, 3
	s_and_b32 s2, s2, -8
	s_ashr_i32 s16, s3, 8
	s_lshl_b32 s48, s14, 10
	s_sub_i32 s2, s43, s2
	s_cmp_lt_i32 s2, 0
	s_cselect_b32 s7, 49, 48
	s_mul_i32 s2, s7, s2
	s_add_i32 s2, s2, s6
	s_mul_hi_i32 s6, s2, 0x2aaaaaab
	s_lshr_b32 s7, s6, 31
	s_ashr_i32 s6, s6, 2
	s_add_i32 s6, s6, s7
	s_lshl_b32 s7, s6, 3
	s_mul_i32 s6, s6, 24
	s_sub_i32 s6, s2, s6
	s_bfe_i32 s2, s6, 0x80000
	s_bfe_u32 s2, s2, 0x3000c
	s_add_i32 s8, s6, s2
	s_bfe_i32 s2, s8, 0x80000
	s_and_b32 s8, s8, 0xf8
	s_sub_i32 s6, s6, s8
	s_sext_i32_i8 s6, s6
	s_add_i32 s26, s7, s6
	s_sext_i32_i16 s2, s2
	s_ashr_i32 s27, s26, 31
	s_lshr_b32 s2, s2, 3
	s_lshl_b64 s[6:7], s[26:27], 19
	s_add_u32 s28, s44, s6
	s_addc_u32 s29, s45, s7
	s_bfe_i64 s[6:7], s[2:3], 0x100000
	v_and_b32_e32 v4, 32, v9
	s_lshl_b64 s[6:7], s[6:7], 19
	v_bitop3_b32 v10, v8, v4, 48 bitop3:0x6c
	s_add_u32 s30, s46, s6
	v_or_b32_e32 v4, v10, v11
	s_addc_u32 s31, s47, s7
	s_add_i32 s27, s48, 0
	v_lshl_or_b32 v132, v1, 11, v4
	s_add_i32 m0, s27, 0x10000
	v_lshl_or_b32 v128, v3, 11, v4
	global_load_lds_dwordx4 v132, s[30:31]
	s_add_i32 m0, s27, 0x12000
	s_add_u32 s6, s30, 0x40000
	global_load_lds_dwordx4 v128, s[30:31]
	s_addc_u32 s7, s31, 0
	s_add_i32 m0, s27, 0x14000
	s_add_i32 s50, s27, 0x2000
	global_load_lds_dwordx4 v132, s[6:7]
	s_add_i32 m0, s27, 0x16000
	v_lshl_or_b32 v134, v0, 11, v4
	global_load_lds_dwordx4 v128, s[6:7]
	s_mov_b32 m0, s27
	s_add_u32 s6, s28, 0x40000
	v_lshl_or_b32 v130, v2, 11, v4
	global_load_lds_dwordx4 v134, s[28:29]
	s_mov_b32 m0, s50
	s_addc_u32 s7, s29, 0
	s_add_i32 s51, s27, 0x4000
	global_load_lds_dwordx4 v130, s[28:29]
	s_mov_b32 m0, s51
	s_add_i32 s52, s27, 0x6000
	global_load_lds_dwordx4 v134, s[6:7]
	s_mov_b32 m0, s52
	v_mov_b32_e32 v133, 0
	global_load_lds_dwordx4 v130, s[6:7]
	v_mov_b32_e32 v129, v133
	v_mov_b32_e32 v135, v133
	v_mov_b32_e32 v131, v133
	s_cmp_eq_u32 s16, 1
	v_lshl_add_u64 v[6:7], s[30:31], 0, v[132:133]
	v_lshl_add_u64 v[4:5], s[30:31], 0, v[128:129]
	v_lshl_add_u64 v[0:1], s[28:29], 0, v[134:135]
	s_cselect_b64 s[6:7], -1, 0
	s_setprio 0
	s_cmp_lg_u32 s16, 1
	v_lshl_add_u64 v[2:3], s[28:29], 0, v[130:131]
	s_cbranch_scc1 .LBB0_1237
	s_setprio 1
	s_barrier

.LBB0_1395:
	s_cmp_gt_i32 s34, 15
	s_cselect_b64 s[2:3], -1, 0
	s_cmp_lt_i32 s35, 16
	s_cselect_b64 s[4:5], -1, 0
	s_or_b64 s[2:3], s[2:3], s[4:5]
	s_and_b64 vcc, exec, s[2:3]
	s_cbranch_vccnz .LBB0_1502
	s_mov_b32 s2, 24
	s_lshl_b32 s2, s2, 3
	s_add_i32 s2, s2, 0
	s_add_i32 s2, s2, 0x201c0
	v_mov_b32_e32 v0, s2
	s_waitcnt vmcnt(0) lgkmcnt(0)
	ds_read_b32 v1, v0
	ds_read_b32 v0, v0 offset:4
	s_load_dword s44, s[0:1], 0xd0
	s_add_u32 s4, s0, 0xd0
	s_addc_u32 s5, s1, 0
	s_mov_b32 s30, s10
	s_and_b32 s45, s33, 0xffffffc0
	s_waitcnt lgkmcnt(0)
	s_mov_b32 s29, s44
	v_readfirstlane_b32 s9, v0
	v_mbcnt_lo_u32_b32 v9, -1, 0
	v_mbcnt_hi_u32_b32 v9, -1, v9
	s_mov_b32 s28, 24
	v_add_u32_e32 v0, s45, v9
	v_readfirstlane_b32 s8, v1
	s_cmpk_gt_i32 s30, 0x2ff
	v_readfirstlane_b32 s2, v0
	s_cbranch_scc1 .LBB0_1412
	s_add_u32 s31, s8, 0x2a000000
	s_addc_u32 s36, s9, 0
	v_lshlrev_b32_e32 v8, 4, v0
	v_lshrrev_b32_e32 v3, 5, v0
	s_add_u32 s37, s8, 0x1500000
	v_bfe_u32 v2, v8, 6, 2
	v_and_b32_e32 v3, 4, v3
	v_and_b32_e32 v4, 48, v0
	v_add_u32_e32 v12, 0x2000, v8
	s_addc_u32 s38, s9, 0
	v_bfe_u32 v1, v0, 2, 26
	v_or3_b32 v2, v2, v3, v4
	v_lshrrev_b32_e32 v4, 6, v12
	s_movk_i32 s6, 0xc0
	v_and_b32_e32 v5, 32, v9
	s_ashr_i32 s40, s30, 31
	v_and_or_b32 v4, v4, s6, v2
	v_bitop3_b32 v5, v8, v5, 48 bitop3:0x6c
	v_and_or_b32 v1, v1, s6, v2
	s_lshr_b32 s6, s40, 29
	v_lshrrev_b32_e32 v3, 7, v12
	v_lshrrev_b32_e32 v10, 1, v5
	v_lshrrev_b32_e32 v5, 1, v0
	v_bfe_u32 v13, v8, 6, 4
	s_mov_b32 s7, 0xfffff0
	v_lshrrev_b32_e32 v0, 3, v0
	s_add_i32 s6, s30, s6
	s_ashr_i32 s12, s2, 6
	v_and_or_b32 v3, v3, s7, v13
	v_and_or_b32 v0, v0, s7, v13
	s_ashr_i32 s7, s6, 3
	s_and_b32 s6, s6, -8
	s_ashr_i32 s3, s2, 8
	s_lshl_b32 s39, s12, 10
	s_sub_i32 s6, s30, s6
	s_cmp_lt_i32 s6, 0
	s_movk_i32 s41, 0x61
	s_cselect_b32 s13, s41, 0x60
	s_mul_i32 s6, s13, s6
	s_add_i32 s6, s6, s7
	s_mul_hi_i32 s7, s6, 0x2aaaaaab
	s_lshr_b32 s13, s7, 31
	s_ashr_i32 s7, s7, 3
	s_add_i32 s7, s7, s13
	s_lshl_b32 s13, s7, 3
	s_mul_i32 s7, s7, 48
	s_sub_i32 s6, s6, s7
	s_bfe_i32 s7, s6, 0x80000
	s_bfe_u32 s7, s7, 0x3000c
	s_add_i32 s7, s6, s7
	s_bfe_i32 s14, s7, 0x80000
	s_and_b32 s7, s7, 0xf8
	s_sub_i32 s6, s6, s7
	s_sext_i32_i8 s6, s6
	s_sext_i32_i16 s15, s14
	s_add_i32 s57, s13, s6
	s_lshr_b32 s14, s15, 3
	s_mul_i32 s7, s57, 0x60000
	s_mul_hi_i32 s6, s57, 0x60000
	s_add_u32 s20, s31, s7
	s_addc_u32 s21, s36, s6
	s_ashr_i32 s6, s15, 3
	v_and_b32_e32 v11, 32, v5
	s_mul_hi_i32 s7, s6, 0x30000
	s_mul_i32 s6, s6, 0x30000
	v_or_b32_e32 v5, v10, v11
	v_mul_u32_u24_e32 v1, 0x180, v1
	s_add_u32 s22, s37, s6
	v_or_b32_e32 v1, v1, v5
	s_addc_u32 s23, s38, s7
	s_add_i32 s42, s39, 0
	v_mul_u32_u24_e32 v4, 0x180, v4
	v_lshlrev_b32_e32 v132, 1, v1
	s_add_i32 m0, s42, 0x10000
	v_or_b32_e32 v4, v4, v5
	global_load_lds_dwordx4 v132, s[22:23]
	s_add_i32 m0, s42, 0x12000
	v_lshlrev_b32_e32 v128, 1, v4
	s_add_u32 s6, s22, 0x1800
	v_mul_u32_u24_e32 v0, 0x300, v0
	global_load_lds_dwordx4 v128, s[22:23]
	s_addc_u32 s7, s23, 0
	s_add_i32 m0, s42, 0x14000
	v_mul_u32_u24_e32 v3, 0x300, v3
	v_or_b32_e32 v0, v0, v5
	global_load_lds_dwordx4 v132, s[6:7]
	s_add_i32 m0, s42, 0x16000
	s_add_i32 s43, s42, 0x2000
	v_or_b32_e32 v3, v3, v5
	v_lshlrev_b32_e32 v134, 1, v0
	global_load_lds_dwordx4 v128, s[6:7]
	s_mov_b32 m0, s42
	s_add_u32 s6, s20, 0x30000
	v_lshlrev_b32_e32 v130, 1, v3
	global_load_lds_dwordx4 v134, s[20:21]
	s_mov_b32 m0, s43
	s_addc_u32 s7, s21, 0
	s_add_i32 s46, s42, 0x4000
	global_load_lds_dwordx4 v130, s[20:21]
	s_mov_b32 m0, s46
	s_add_i32 s47, s42, 0x6000
	global_load_lds_dwordx4 v134, s[6:7]
	s_mov_b32 m0, s47
	v_mov_b32_e32 v133, 0
	global_load_lds_dwordx4 v130, s[6:7]
	v_mov_b32_e32 v129, v133
	v_mov_b32_e32 v135, v133
	v_mov_b32_e32 v131, v133
	s_cmp_eq_u32 s3, 1
	s_movk_i32 s16, 0x300
	v_lshl_add_u64 v[6:7], s[22:23], 0, v[132:133]
	v_lshl_add_u64 v[4:5], s[22:23], 0, v[128:129]
	v_lshl_add_u64 v[0:1], s[20:21], 0, v[134:135]
	s_cselect_b64 s[6:7], -1, 0
	s_setprio 0
	s_cmp_lg_u32 s3, 1
	v_lshl_add_u64 v[2:3], s[20:21], 0, v[130:131]
	s_cbranch_scc1 .LBB0_1399
	s_setprio 1
	s_barrier

.LBB0_1417:
	v_lshlrev_b32_e32 v1, 4, v0
	v_and_b32_e32 v2, 32, v8
	v_bitop3_b32 v2, v1, v2, 48 bitop3:0x6c
	s_add_u32 s49, s8, 0x2a000300
	v_lshrrev_b32_e32 v5, 1, v0
	v_lshrrev_b32_e32 v2, 1, v2
	s_addc_u32 s50, s9, 0
	v_bfe_u32 v3, v0, 2, 26
	v_bfe_u32 v4, v1, 6, 4
	v_and_or_b32 v2, v5, 32, v2
	v_and_b32_e32 v5, 48, v0
	v_lshrrev_b32_e32 v6, 5, v0
	v_lshrrev_b32_e32 v0, 3, v0
	s_mov_b32 s3, 0xfffff0
	s_add_u32 s51, s8, 0x1800000
	v_and_or_b32 v0, v0, s3, v4
	s_addc_u32 s52, s9, 0
	v_and_b32_e32 v6, 4, v6
	v_bfe_u32 v7, v1, 6, 2
	v_mul_u32_u24_e32 v0, 0x300, v0
	s_add_i32 s2, s6, s2
	v_or3_b32 v5, v7, v6, v5
	s_movk_i32 s7, 0xc0
	v_or_b32_e32 v0, v0, v2
	s_ashr_i32 s6, s2, 31
	v_and_or_b32 v3, v3, s7, v5
	v_lshlrev_b32_e32 v128, 1, v0
	v_lshlrev_b32_e32 v0, 1, v2
	v_add_u32_e32 v1, 0x2000, v1
	s_lshr_b32 s6, s6, 26
	v_lshl_or_b32 v130, v3, 9, v0
	v_lshrrev_b32_e32 v3, 7, v1
	v_lshrrev_b32_e32 v1, 6, v1
	s_add_i32 s6, s2, s6
	v_and_or_b32 v1, v1, s7, v5
	s_ashr_i32 s7, s6, 6
	s_and_b32 s6, s6, 0xffc0
	s_sub_i32 s6, s2, s6
	s_bfe_i32 s2, s6, 0x80000
	s_bfe_u32 s2, s2, 0x3000c
	s_add_i32 s13, s6, s2
	s_bfe_i32 s2, s13, 0x80000
	s_and_b32 s13, s13, 0xf8
	s_sub_i32 s6, s6, s13
	s_lshl_b32 s7, s7, 3
	s_sext_i32_i8 s6, s6
	s_ashr_i32 s12, s14, 6
	s_sext_i32_i16 s2, s2
	s_add_i32 s68, s7, s6
	v_and_or_b32 v3, v3, s3, v4
	s_ashr_i32 s3, s14, 8
	s_lshl_b32 s53, s12, 10
	s_lshr_b32 s2, s2, 3
	s_mul_i32 s7, s68, 0x60000
	s_mul_hi_i32 s6, s68, 0x60000
	s_add_u32 s22, s49, s7
	s_addc_u32 s23, s50, s6
	s_bfe_i64 s[6:7], s[2:3], 0x100000
	s_lshl_b64 s[6:7], s[6:7], 17
	s_add_u32 s24, s51, s6
	s_addc_u32 s25, s52, s7
	s_add_i32 s54, s53, 0
	s_add_i32 m0, s54, 0x10000
	v_lshl_or_b32 v134, v1, 9, v0
	global_load_lds_dwordx4 v130, s[24:25]
	s_add_i32 m0, s54, 0x12000
	s_add_u32 s6, s24, 0x1000
	global_load_lds_dwordx4 v134, s[24:25]
	s_addc_u32 s7, s25, 0
	s_add_i32 m0, s54, 0x14000
	v_mul_u32_u24_e32 v3, 0x300, v3
	global_load_lds_dwordx4 v130, s[6:7]
	s_add_i32 m0, s54, 0x16000
	s_add_i32 s55, s54, 0x2000
	v_or_b32_e32 v2, v3, v2
	global_load_lds_dwordx4 v134, s[6:7]
	s_mov_b32 m0, s54
	s_add_u32 s6, s22, 0x30000
	v_lshlrev_b32_e32 v132, 1, v2
	global_load_lds_dwordx4 v128, s[22:23]
	s_mov_b32 m0, s55
	s_addc_u32 s7, s23, 0
	s_add_i32 s56, s54, 0x4000
	global_load_lds_dwordx4 v132, s[22:23]
	s_mov_b32 m0, s56
	s_add_i32 s57, s54, 0x6000
	global_load_lds_dwordx4 v128, s[6:7]
	s_mov_b32 m0, s57
	v_mov_b32_e32 v131, 0
	global_load_lds_dwordx4 v132, s[6:7]
	v_mov_b32_e32 v135, v131
	v_mov_b32_e32 v129, v131
	v_mov_b32_e32 v133, v131
	s_cmp_eq_u32 s3, 1
	s_mov_b32 s58, 0
	v_lshl_add_u64 v[6:7], s[24:25], 0, v[130:131]
	v_lshl_add_u64 v[4:5], s[24:25], 0, v[134:135]
	v_lshl_add_u64 v[0:1], s[22:23], 0, v[128:129]
	s_cselect_b64 s[6:7], -1, 0
	s_setprio 0
	s_cmp_lg_u32 s3, 1
	v_lshl_add_u64 v[2:3], s[22:23], 0, v[132:133]
	s_cbranch_scc1 .LBB0_1419
	s_setprio 1
	s_barrier

.LBB0_1614:
	s_mul_i32 s14, s13, 0x3400
	s_and_b32 s7, 1, s18
	s_add_i32 s14, s14, 0
	s_andn2_b32 s15, 1, s18
	s_mul_i32 s6, s17, 0x3400
	s_cmpk_lt_u32 s18, 0xfc
	s_cselect_b32 s21, s20, 0x2fd000
	s_cmp_eq_u32 s7, 1
	s_setprio 0
	v_add_u32_e32 v96, s14, v199
	s_waitcnt lgkmcnt(6)
	v_mfma_scale_f32_32x32x64_f8f6f4 v[80:95], v[168:175], v[136:143], v[64:79], v191, v190 op_sel_hi:[0,0,0]
	s_waitcnt vmcnt(2)
	ds_write_b128 v96, v[180:183] offset:20480
	v_add_u32_e32 v96, s14, v200
	s_mulk_i32 s15, 0x2800
	s_waitcnt vmcnt(1)
	ds_write_b64 v96, v[188:189] offset:28672
	v_add_u32_e32 v96, s15, v205
	s_mov_b32 s39, s31
	s_waitcnt vmcnt(0)
	ds_write_b128 v96, v[176:179]
	buffer_load_dwordx4 v[180:183], v203, s[28:31], s21 offen
	buffer_load_dwordx2 v[188:189], v202, s[28:31], s21 offen
	buffer_load_dwordx4 v[176:179], v203, s[36:39], s19 offen
	v_add_u32_e32 v172, s6, v204
	s_cselect_b32 s6, 0x2800, 0
	v_add_u32_e32 v186, s6, v198
	s_waitcnt lgkmcnt(7)
	v_mfma_scale_f32_32x32x64_f8f6f4 v[96:111], v[160:167], v[136:143], v[64:79], v191, v190 op_sel_hi:[0,0,0]
	ds_read_b128 v[160:163], v172 offset:20608
	ds_read_b128 v[164:167], v172 offset:20624
	ds_read_b128 v[168:171], v172 offset:27264
	ds_read_b128 v[172:175], v172 offset:27280
	s_waitcnt lgkmcnt(9)
	v_mfma_scale_f32_32x32x64_f8f6f4 v[80:95], v[152:159], v[128:135], v[80:95], v191, v190 op_sel_hi:[0,0,0]
	ds_read_b128 v[152:155], v186
	ds_read_b128 v[156:159], v186 offset:16
	ds_read_b128 v[206:209], v186 offset:2560
	ds_read_b128 v[210:213], v186 offset:2576
	s_waitcnt lgkmcnt(11)
	v_mfma_scale_f32_32x32x64_f8f6f4 v[96:111], v[144:151], v[128:135], v[96:111], v191, v190 op_sel_hi:[0,0,0]
	ds_read_b128 v[144:147], v186 offset:5120
	ds_read_b128 v[148:151], v186 offset:5136
	ds_read_b128 v[214:217], v186 offset:7680
	ds_read_b128 v[218:221], v186 offset:7696
	s_waitcnt lgkmcnt(10)
	v_mfma_scale_f32_32x32x64_f8f6f4 v[80:95], v[160:167], v[120:127], v[80:95], v191, v190 op_sel_hi:[0,0,0]
	s_waitcnt lgkmcnt(8)
	v_mfma_scale_f32_32x32x64_f8f6f4 v[96:111], v[168:175], v[120:127], v[96:111], v191, v190 op_sel_hi:[0,0,0]
	s_waitcnt lgkmcnt(6)
	v_mfma_f32_32x32x64_f8f6f4 v[0:15], v[112:119], v[152:159], v[0:15]
	s_waitcnt lgkmcnt(4)
	v_mfma_f32_32x32x64_f8f6f4 v[16:31], v[112:119], v[206:213], v[16:31]
	s_waitcnt lgkmcnt(2)
	v_mfma_f32_32x32x64_f8f6f4 v[32:47], v[112:119], v[144:151], v[32:47]
	s_waitcnt lgkmcnt(0)
	v_mfma_f32_32x32x64_f8f6f4 v[48:63], v[112:119], v[214:221], v[48:63]
	v_cndmask_b32_e64 v144, 0, 1, s[46:47]
	v_cmp_ne_u32_e64 s[6:7], 1, v144
	s_andn2_b64 vcc, exec, s[46:47]
	s_cbranch_vccnz .LBB0_1616
	s_barrier

.LBB0_1823:
	v_lshlrev_b32_e32 v4, 4, v80
	v_and_b32_e32 v0, 32, v8
	v_bfe_u32 v7, v80, 2, 4
	v_bitop3_b32 v5, v4, v0, 48 bitop3:0x6c
	v_and_b32_e32 v6, 64, v80
	v_lshrrev_b32_e32 v1, 3, v80
	s_mov_b32 s3, 0x1ffff0
	v_or_b32_e32 v0, v5, v6
	v_and_or_b32 v1, v1, s3, v7
	v_add_u32_e32 v9, 0x2000, v4
	s_ashr_i32 s2, s4, 6
	v_lshl_or_b32 v64, v1, 11, v0
	v_lshrrev_b32_e32 v1, 7, v9
	v_and_or_b32 v1, v1, s3, v7
	s_ashr_i32 s3, s4, 8
	s_lshl_b32 s50, s2, 10
	s_add_u32 s51, s30, 0x26000000
	s_addc_u32 s52, s31, 0
	s_add_u32 s12, s30, 0x1e80000
	s_addc_u32 s13, s31, 0
	s_add_i32 s8, s5, s8
	s_ashr_i32 s9, s8, 31
	s_lshl_b64 s[14:15], s[8:9], 19
	s_add_u32 s22, s51, s14
	s_addc_u32 s23, s52, s15
	s_add_i32 s9, s50, 0
	s_add_i32 m0, s9, 0x10000
	v_lshl_or_b32 v66, v1, 11, v0
	global_load_lds_dwordx4 v64, s[12:13]
	s_add_i32 m0, s9, 0x12000
	s_add_u32 s14, s30, 0x1ec0000
	s_addc_u32 s15, s31, 0
	s_add_i32 s53, s9, 0x14000
	global_load_lds_dwordx4 v66, s[12:13]
	s_mov_b32 m0, s53
	s_add_i32 s54, s9, 0x16000
	global_load_lds_dwordx4 v64, s[14:15]
	s_mov_b32 m0, s54
	s_add_i32 s56, s9, 0x2000
	global_load_lds_dwordx4 v66, s[14:15]
	s_mov_b32 m0, s9
	s_add_u32 s14, s22, 0x40000
	global_load_lds_dwordx4 v64, s[22:23]
	s_mov_b32 m0, s56
	s_addc_u32 s15, s23, 0
	s_add_i32 s57, s9, 0x4000
	global_load_lds_dwordx4 v66, s[22:23]
	s_mov_b32 m0, s57
	s_add_i32 s58, s9, 0x6000
	global_load_lds_dwordx4 v64, s[14:15]
	s_mov_b32 m0, s58
	v_mov_b32_e32 v65, 0
	global_load_lds_dwordx4 v66, s[14:15]
	v_mov_b32_e32 v67, v65
	s_cmp_eq_u32 s3, 1
	s_mov_b32 s64, 0
	v_lshl_add_u64 v[0:1], s[22:23], 0, v[64:65]
	s_cselect_b64 s[14:15], -1, 0
	s_setprio 0
	s_cmp_lg_u32 s3, 1
	v_lshl_add_u64 v[2:3], s[22:23], 0, v[66:67]
	s_cbranch_scc1 .LBB0_1825
	s_setprio 1
	s_barrier

.LBB0_2523:
	s_cmp_gt_i32 s34, 26
	s_cselect_b64 s[2:3], -1, 0
	s_cmp_lt_i32 s35, 27
	s_cselect_b64 s[4:5], -1, 0
	s_or_b64 s[2:3], s[2:3], s[4:5]
	s_and_b64 vcc, exec, s[2:3]
	s_cbranch_vccnz .LBB0_2610
	s_mov_b32 s2, 24
	s_lshl_b32 s2, s2, 3
	s_add_i32 s2, s2, 0
	s_add_i32 s2, s2, 0x201c0
	v_mov_b32_e32 v0, s2
	s_waitcnt vmcnt(0) lgkmcnt(0)
	ds_read_b32 v1, v0
	ds_read_b32 v0, v0 offset:4
	s_load_dword s42, s[0:1], 0xd0
	s_add_u32 s4, s0, 0xd0
	s_addc_u32 s5, s1, 0
	s_mov_b32 s45, s10
	s_and_b32 s43, s33, 0xffffffc0
	s_waitcnt lgkmcnt(0)
	s_mov_b32 s44, s42
	v_readfirstlane_b32 s15, v0
	v_mbcnt_lo_u32_b32 v9, -1, 0
	v_mbcnt_hi_u32_b32 v9, -1, v9
	v_readfirstlane_b32 s14, v1
	v_add_u32_e32 v0, s43, v9
	s_cmpk_gt_i32 s45, 0x5ff
	v_readfirstlane_b32 s3, v0
	s_cbranch_scc1 .LBB0_2544
	s_add_u32 s46, s14, 0x26000000
	s_addc_u32 s47, s15, 0
	v_lshlrev_b32_e32 v8, 4, v0
	v_lshrrev_b32_e32 v1, 5, v0
	v_lshrrev_b32_e32 v3, 1, v0
	s_add_u32 s48, s14, 0x800000
	v_and_b32_e32 v1, 4, v1
	v_bfe_u32 v2, v8, 6, 2
	v_and_b32_e32 v3, 24, v3
	v_add_u32_e32 v12, 0x2000, v8
	s_addc_u32 s49, s15, 0
	v_or3_b32 v1, v1, v2, v3
	v_lshrrev_b32_e32 v2, 7, v12
	s_mov_b32 s2, 0x1fffe0
	v_and_b32_e32 v11, 64, v0
	v_bfe_u32 v0, v0, 3, 25
	s_ashr_i32 s51, s45, 31
	v_and_or_b32 v3, v2, s2, v1
	v_and_or_b32 v1, v0, s2, v1
	s_lshr_b32 s2, s51, 29
	v_bfe_u32 v13, v8, 6, 4
	s_mov_b32 s6, 0x1ffff0
	s_add_i32 s2, s45, s2
	s_ashr_i32 s16, s3, 6
	v_and_or_b32 v2, v2, s6, v13
	v_and_or_b32 v0, v0, s6, v13
	s_ashr_i32 s6, s2, 3
	s_and_b32 s2, s2, -8
	s_ashr_i32 s18, s3, 8
	s_lshl_b32 s50, s16, 10
	s_sub_i32 s2, s45, s2
	s_cmp_lt_i32 s2, 0
	s_movk_i32 s52, 0xc1
	s_cselect_b32 s7, s52, 0xc0
	s_mul_i32 s2, s7, s2
	s_add_i32 s2, s2, s6
	s_mul_hi_i32 s6, s2, 0x2aaaaaab
	s_lshr_b32 s7, s6, 31
	s_ashr_i32 s6, s6, 4
	s_add_i32 s6, s6, s7
	s_lshl_b32 s7, s6, 3
	s_mulk_i32 s6, 0x60
	s_sub_i32 s6, s2, s6
	s_bfe_i32 s2, s6, 0x80000
	s_bfe_u32 s2, s2, 0x3000c
	s_add_i32 s8, s6, s2
	s_bfe_i32 s2, s8, 0x80000
	s_and_b32 s8, s8, 0xf8
	s_sub_i32 s6, s6, s8
	s_sext_i32_i8 s6, s6
	s_add_i32 s28, s7, s6
	s_sext_i32_i16 s2, s2
	s_ashr_i32 s29, s28, 31
	s_lshr_b32 s2, s2, 3
	s_lshl_b64 s[6:7], s[28:29], 19
	s_add_u32 s30, s46, s6
	s_addc_u32 s31, s47, s7
	s_bfe_i64 s[6:7], s[2:3], 0x100000
	v_and_b32_e32 v4, 32, v9
	s_lshl_b64 s[6:7], s[6:7], 19
	v_bitop3_b32 v10, v8, v4, 48 bitop3:0x6c
	s_add_u32 s36, s48, s6
	v_or_b32_e32 v4, v10, v11
	s_addc_u32 s37, s49, s7
	s_add_i32 s53, s50, 0
	v_lshl_or_b32 v132, v1, 11, v4
	s_add_i32 m0, s53, 0x10000
	v_lshl_or_b32 v128, v3, 11, v4
	global_load_lds_dwordx4 v132, s[36:37]
	s_add_i32 m0, s53, 0x12000
	s_add_u32 s6, s36, 0x40000
	global_load_lds_dwordx4 v128, s[36:37]
	s_addc_u32 s7, s37, 0
	s_add_i32 m0, s53, 0x14000
	s_add_i32 s54, s53, 0x2000
	global_load_lds_dwordx4 v132, s[6:7]
	s_add_i32 m0, s53, 0x16000
	v_lshl_or_b32 v134, v0, 11, v4
	global_load_lds_dwordx4 v128, s[6:7]
	s_mov_b32 m0, s53
	s_add_u32 s6, s30, 0x40000
	v_lshl_or_b32 v130, v2, 11, v4
	global_load_lds_dwordx4 v134, s[30:31]
	s_mov_b32 m0, s54
	s_addc_u32 s7, s31, 0
	s_add_i32 s55, s53, 0x4000
	global_load_lds_dwordx4 v130, s[30:31]
	s_mov_b32 m0, s55
	s_add_i32 s56, s53, 0x6000
	global_load_lds_dwordx4 v134, s[6:7]
	s_mov_b32 m0, s56
	v_mov_b32_e32 v137, 0
	global_load_lds_dwordx4 v130, s[6:7]
	v_mov_b32_e32 v133, v137
	v_mov_b32_e32 v129, v137
	v_mov_b32_e32 v135, v137
	v_mov_b32_e32 v131, v137
	s_cmp_eq_u32 s18, 1
	v_lshl_add_u64 v[6:7], s[36:37], 0, v[132:133]
	v_lshl_add_u64 v[4:5], s[36:37], 0, v[128:129]
	v_lshl_add_u64 v[0:1], s[30:31], 0, v[134:135]
	s_cselect_b64 s[6:7], -1, 0
	s_setprio 0
	s_cmp_lg_u32 s18, 1
	v_lshl_add_u64 v[2:3], s[30:31], 0, v[130:131]
	s_cbranch_scc1 .LBB0_2527
	s_setprio 1
	s_barrier

.LBB0_2807:
	v_lshlrev_b32_e32 v4, 4, v80
	v_and_b32_e32 v0, 32, v8
	v_bfe_u32 v7, v80, 2, 4
	v_bitop3_b32 v5, v4, v0, 48 bitop3:0x6c
	v_and_b32_e32 v6, 64, v80
	v_lshrrev_b32_e32 v1, 3, v80
	s_mov_b32 s3, 0x1ffff0
	v_or_b32_e32 v0, v5, v6
	v_and_or_b32 v1, v1, s3, v7
	v_add_u32_e32 v9, 0x2000, v4
	s_ashr_i32 s2, s4, 6
	v_lshl_or_b32 v64, v1, 11, v0
	v_lshrrev_b32_e32 v1, 7, v9
	v_and_or_b32 v1, v1, s3, v7
	s_ashr_i32 s3, s4, 8
	s_lshl_b32 s50, s2, 10
	s_add_u32 s51, s30, 0x26000000
	s_addc_u32 s52, s31, 0
	s_add_u32 s12, s30, 0x1f00000
	s_addc_u32 s13, s31, 0
	s_add_i32 s8, s5, s8
	s_ashr_i32 s9, s8, 31
	s_lshl_b64 s[14:15], s[8:9], 19
	s_add_u32 s22, s51, s14
	s_addc_u32 s23, s52, s15
	s_add_i32 s9, s50, 0
	s_add_i32 m0, s9, 0x10000
	v_lshl_or_b32 v66, v1, 11, v0
	global_load_lds_dwordx4 v64, s[12:13]
	s_add_i32 m0, s9, 0x12000
	s_add_u32 s14, s30, 0x1f40000
	s_addc_u32 s15, s31, 0
	s_add_i32 s53, s9, 0x14000
	global_load_lds_dwordx4 v66, s[12:13]
	s_mov_b32 m0, s53
	s_add_i32 s54, s9, 0x16000
	global_load_lds_dwordx4 v64, s[14:15]
	s_mov_b32 m0, s54
	s_add_i32 s56, s9, 0x2000
	global_load_lds_dwordx4 v66, s[14:15]
	s_mov_b32 m0, s9
	s_add_u32 s14, s22, 0x40000
	global_load_lds_dwordx4 v64, s[22:23]
	s_mov_b32 m0, s56
	s_addc_u32 s15, s23, 0
	s_add_i32 s57, s9, 0x4000
	global_load_lds_dwordx4 v66, s[22:23]
	s_mov_b32 m0, s57
	s_add_i32 s58, s9, 0x6000
	global_load_lds_dwordx4 v64, s[14:15]
	s_mov_b32 m0, s58
	v_mov_b32_e32 v65, 0
	global_load_lds_dwordx4 v66, s[14:15]
	v_mov_b32_e32 v67, v65
	s_cmp_eq_u32 s3, 1
	s_mov_b32 s64, 0
	v_lshl_add_u64 v[0:1], s[22:23], 0, v[64:65]
	s_cselect_b64 s[14:15], -1, 0
	s_setprio 0
	s_cmp_lg_u32 s3, 1
	v_lshl_add_u64 v[2:3], s[22:23], 0, v[66:67]
	s_cbranch_scc1 .LBB0_2809
	s_setprio 1
	s_barrier

.LBB0_3507:
	s_cmp_gt_i32 s34, 38
	s_cselect_b64 s[2:3], -1, 0
	s_cmp_lt_i32 s35, 39
	s_cselect_b64 s[4:5], -1, 0
	s_or_b64 s[2:3], s[2:3], s[4:5]
	s_and_b64 vcc, exec, s[2:3]
	s_cbranch_vccnz .LBB0_3669
	s_mov_b32 s2, 24
	s_lshl_b32 s2, s2, 3
	s_add_i32 s2, s2, 0
	s_add_i32 s2, s2, 0x201c0
	v_mov_b32_e32 v0, s2
	s_waitcnt vmcnt(0) lgkmcnt(0)
	ds_read_b32 v1, v0
	ds_read_b32 v0, v0 offset:4
	s_load_dword s40, s[0:1], 0xd0
	s_add_u32 s4, s0, 0xd0
	s_addc_u32 s5, s1, 0
	s_mov_b32 s43, s10
	s_and_b32 s41, s33, 0xffffffc0
	s_waitcnt lgkmcnt(0)
	s_mov_b32 s42, s40
	v_readfirstlane_b32 s13, v0
	v_mbcnt_lo_u32_b32 v9, -1, 0
	v_mbcnt_hi_u32_b32 v9, -1, v9
	v_readfirstlane_b32 s12, v1
	v_add_u32_e32 v0, s41, v9
	s_cmpk_gt_i32 s43, 0x17f
	v_readfirstlane_b32 s3, v0
	s_cbranch_scc1 .LBB0_3524
	s_add_u32 s44, s12, 0x26000000
	s_addc_u32 s45, s13, 0
	v_lshlrev_b32_e32 v8, 4, v0
	v_lshrrev_b32_e32 v1, 5, v0
	v_lshrrev_b32_e32 v3, 1, v0
	s_add_u32 s46, s12, 0x1380000
	v_and_b32_e32 v1, 4, v1
	v_bfe_u32 v2, v8, 6, 2
	v_and_b32_e32 v3, 24, v3
	v_add_u32_e32 v12, 0x2000, v8
	s_addc_u32 s47, s13, 0
	v_or3_b32 v1, v1, v2, v3
	v_lshrrev_b32_e32 v2, 7, v12
	s_mov_b32 s2, 0x1fffe0
	v_and_b32_e32 v11, 64, v0
	v_bfe_u32 v0, v0, 3, 25
	s_ashr_i32 s49, s43, 31
	v_and_or_b32 v3, v2, s2, v1
	v_and_or_b32 v1, v0, s2, v1
	s_lshr_b32 s2, s49, 29
	v_bfe_u32 v13, v8, 6, 4
	s_mov_b32 s6, 0x1ffff0
	s_add_i32 s2, s43, s2
	s_ashr_i32 s14, s3, 6
	v_and_or_b32 v2, v2, s6, v13
	v_and_or_b32 v0, v0, s6, v13
	s_ashr_i32 s6, s2, 3
	s_and_b32 s2, s2, -8
	s_ashr_i32 s16, s3, 8
	s_lshl_b32 s48, s14, 10
	s_sub_i32 s2, s43, s2
	s_cmp_lt_i32 s2, 0
	s_cselect_b32 s7, 49, 48
	s_mul_i32 s2, s7, s2
	s_add_i32 s2, s2, s6
	s_mul_hi_i32 s6, s2, 0x2aaaaaab
	s_lshr_b32 s7, s6, 31
	s_ashr_i32 s6, s6, 2
	s_add_i32 s6, s6, s7
	s_lshl_b32 s7, s6, 3
	s_mul_i32 s6, s6, 24
	s_sub_i32 s6, s2, s6
	s_bfe_i32 s2, s6, 0x80000
	s_bfe_u32 s2, s2, 0x3000c
	s_add_i32 s8, s6, s2
	s_bfe_i32 s2, s8, 0x80000
	s_and_b32 s8, s8, 0xf8
	s_sub_i32 s6, s6, s8
	s_sext_i32_i8 s6, s6
	s_add_i32 s26, s7, s6
	s_sext_i32_i16 s2, s2
	s_ashr_i32 s27, s26, 31
	s_lshr_b32 s2, s2, 3
	s_lshl_b64 s[6:7], s[26:27], 19
	s_add_u32 s28, s44, s6
	s_addc_u32 s29, s45, s7
	s_bfe_i64 s[6:7], s[2:3], 0x100000
	v_and_b32_e32 v4, 32, v9
	s_lshl_b64 s[6:7], s[6:7], 19
	v_bitop3_b32 v10, v8, v4, 48 bitop3:0x6c
	s_add_u32 s30, s46, s6
	v_or_b32_e32 v4, v10, v11
	s_addc_u32 s31, s47, s7
	s_add_i32 s27, s48, 0
	v_lshl_or_b32 v132, v1, 11, v4
	s_add_i32 m0, s27, 0x10000
	v_lshl_or_b32 v128, v3, 11, v4
	global_load_lds_dwordx4 v132, s[30:31]
	s_add_i32 m0, s27, 0x12000
	s_add_u32 s6, s30, 0x40000
	global_load_lds_dwordx4 v128, s[30:31]
	s_addc_u32 s7, s31, 0
	s_add_i32 m0, s27, 0x14000
	s_add_i32 s50, s27, 0x2000
	global_load_lds_dwordx4 v132, s[6:7]
	s_add_i32 m0, s27, 0x16000
	v_lshl_or_b32 v134, v0, 11, v4
	global_load_lds_dwordx4 v128, s[6:7]
	s_mov_b32 m0, s27
	s_add_u32 s6, s28, 0x40000
	v_lshl_or_b32 v130, v2, 11, v4
	global_load_lds_dwordx4 v134, s[28:29]
	s_mov_b32 m0, s50
	s_addc_u32 s7, s29, 0
	s_add_i32 s51, s27, 0x4000
	global_load_lds_dwordx4 v130, s[28:29]
	s_mov_b32 m0, s51
	s_add_i32 s52, s27, 0x6000
	global_load_lds_dwordx4 v134, s[6:7]
	s_mov_b32 m0, s52
	v_mov_b32_e32 v133, 0
	global_load_lds_dwordx4 v130, s[6:7]
	v_mov_b32_e32 v129, v133
	v_mov_b32_e32 v135, v133
	v_mov_b32_e32 v131, v133
	s_cmp_eq_u32 s16, 1
	v_lshl_add_u64 v[6:7], s[30:31], 0, v[132:133]
	v_lshl_add_u64 v[4:5], s[30:31], 0, v[128:129]
	v_lshl_add_u64 v[0:1], s[28:29], 0, v[134:135]
	s_cselect_b64 s[6:7], -1, 0
	s_setprio 0
	s_cmp_lg_u32 s16, 1
	v_lshl_add_u64 v[2:3], s[28:29], 0, v[130:131]
	s_cbranch_scc1 .LBB0_3511
	s_setprio 1
	s_barrier

.LBB0_3669:
	s_cmp_gt_i32 s34, 39
	s_cselect_b64 s[2:3], -1, 0
	s_cmp_lt_i32 s35, 40
	s_cselect_b64 s[4:5], -1, 0
	s_or_b64 s[2:3], s[2:3], s[4:5]
	s_and_b64 vcc, exec, s[2:3]
	s_cbranch_vccnz .LBB0_3776
	s_mov_b32 s2, 24
	s_lshl_b32 s2, s2, 3
	s_add_i32 s2, s2, 0
	s_add_i32 s2, s2, 0x201c0
	v_mov_b32_e32 v0, s2
	s_waitcnt vmcnt(0) lgkmcnt(0)
	ds_read_b32 v1, v0
	ds_read_b32 v0, v0 offset:4
	s_load_dword s44, s[0:1], 0xd0
	s_add_u32 s4, s0, 0xd0
	s_addc_u32 s5, s1, 0
	s_mov_b32 s30, s10
	s_and_b32 s45, s33, 0xffffffc0
	s_waitcnt lgkmcnt(0)
	s_mov_b32 s29, s44
	v_readfirstlane_b32 s9, v0
	v_mbcnt_lo_u32_b32 v9, -1, 0
	v_mbcnt_hi_u32_b32 v9, -1, v9
	s_mov_b32 s28, 24
	v_add_u32_e32 v0, s45, v9
	v_readfirstlane_b32 s8, v1
	s_cmpk_gt_i32 s30, 0x2ff
	v_readfirstlane_b32 s2, v0
	s_cbranch_scc1 .LBB0_3686
	s_add_u32 s31, s8, 0x2a000000
	s_addc_u32 s36, s9, 0
	v_lshlrev_b32_e32 v8, 4, v0
	v_lshrrev_b32_e32 v3, 5, v0
	s_add_u32 s37, s8, 0x1680000
	v_bfe_u32 v2, v8, 6, 2
	v_and_b32_e32 v3, 4, v3
	v_and_b32_e32 v4, 48, v0
	v_add_u32_e32 v12, 0x2000, v8
	s_addc_u32 s38, s9, 0
	v_bfe_u32 v1, v0, 2, 26
	v_or3_b32 v2, v2, v3, v4
	v_lshrrev_b32_e32 v4, 6, v12
	s_movk_i32 s6, 0xc0
	v_and_b32_e32 v5, 32, v9
	s_ashr_i32 s40, s30, 31
	v_and_or_b32 v4, v4, s6, v2
	v_bitop3_b32 v5, v8, v5, 48 bitop3:0x6c
	v_and_or_b32 v1, v1, s6, v2
	s_lshr_b32 s6, s40, 29
	v_lshrrev_b32_e32 v3, 7, v12
	v_lshrrev_b32_e32 v10, 1, v5
	v_lshrrev_b32_e32 v5, 1, v0
	v_bfe_u32 v13, v8, 6, 4
	s_mov_b32 s7, 0xfffff0
	v_lshrrev_b32_e32 v0, 3, v0
	s_add_i32 s6, s30, s6
	s_ashr_i32 s12, s2, 6
	v_and_or_b32 v3, v3, s7, v13
	v_and_or_b32 v0, v0, s7, v13
	s_ashr_i32 s7, s6, 3
	s_and_b32 s6, s6, -8
	s_ashr_i32 s3, s2, 8
	s_lshl_b32 s39, s12, 10
	s_sub_i32 s6, s30, s6
	s_cmp_lt_i32 s6, 0
	s_movk_i32 s41, 0x61
	s_cselect_b32 s13, s41, 0x60
	s_mul_i32 s6, s13, s6
	s_add_i32 s6, s6, s7
	s_mul_hi_i32 s7, s6, 0x2aaaaaab
	s_lshr_b32 s13, s7, 31
	s_ashr_i32 s7, s7, 3
	s_add_i32 s7, s7, s13
	s_lshl_b32 s13, s7, 3
	s_mul_i32 s7, s7, 48
	s_sub_i32 s6, s6, s7
	s_bfe_i32 s7, s6, 0x80000
	s_bfe_u32 s7, s7, 0x3000c
	s_add_i32 s7, s6, s7
	s_bfe_i32 s14, s7, 0x80000
	s_and_b32 s7, s7, 0xf8
	s_sub_i32 s6, s6, s7
	s_sext_i32_i8 s6, s6
	s_sext_i32_i16 s15, s14
	s_add_i32 s57, s13, s6
	s_lshr_b32 s14, s15, 3
	s_mul_i32 s7, s57, 0x60000
	s_mul_hi_i32 s6, s57, 0x60000
	s_add_u32 s20, s31, s7
	s_addc_u32 s21, s36, s6
	s_ashr_i32 s6, s15, 3
	v_and_b32_e32 v11, 32, v5
	s_mul_hi_i32 s7, s6, 0x30000
	s_mul_i32 s6, s6, 0x30000
	v_or_b32_e32 v5, v10, v11
	v_mul_u32_u24_e32 v1, 0x180, v1
	s_add_u32 s22, s37, s6
	v_or_b32_e32 v1, v1, v5
	s_addc_u32 s23, s38, s7
	s_add_i32 s42, s39, 0
	v_mul_u32_u24_e32 v4, 0x180, v4
	v_lshlrev_b32_e32 v132, 1, v1
	s_add_i32 m0, s42, 0x10000
	v_or_b32_e32 v4, v4, v5
	global_load_lds_dwordx4 v132, s[22:23]
	s_add_i32 m0, s42, 0x12000
	v_lshlrev_b32_e32 v128, 1, v4
	s_add_u32 s6, s22, 0x1800
	v_mul_u32_u24_e32 v0, 0x300, v0
	global_load_lds_dwordx4 v128, s[22:23]
	s_addc_u32 s7, s23, 0
	s_add_i32 m0, s42, 0x14000
	v_mul_u32_u24_e32 v3, 0x300, v3
	v_or_b32_e32 v0, v0, v5
	global_load_lds_dwordx4 v132, s[6:7]
	s_add_i32 m0, s42, 0x16000
	s_add_i32 s43, s42, 0x2000
	v_or_b32_e32 v3, v3, v5
	v_lshlrev_b32_e32 v134, 1, v0
	global_load_lds_dwordx4 v128, s[6:7]
	s_mov_b32 m0, s42
	s_add_u32 s6, s20, 0x30000
	v_lshlrev_b32_e32 v130, 1, v3
	global_load_lds_dwordx4 v134, s[20:21]
	s_mov_b32 m0, s43
	s_addc_u32 s7, s21, 0
	s_add_i32 s46, s42, 0x4000
	global_load_lds_dwordx4 v130, s[20:21]
	s_mov_b32 m0, s46
	s_add_i32 s47, s42, 0x6000
	global_load_lds_dwordx4 v134, s[6:7]
	s_mov_b32 m0, s47
	v_mov_b32_e32 v133, 0
	global_load_lds_dwordx4 v130, s[6:7]
	v_mov_b32_e32 v129, v133
	v_mov_b32_e32 v135, v133
	v_mov_b32_e32 v131, v133
	s_cmp_eq_u32 s3, 1
	s_movk_i32 s16, 0x300
	v_lshl_add_u64 v[6:7], s[22:23], 0, v[132:133]
	v_lshl_add_u64 v[4:5], s[22:23], 0, v[128:129]
	v_lshl_add_u64 v[0:1], s[20:21], 0, v[134:135]
	s_cselect_b64 s[6:7], -1, 0
	s_setprio 0
	s_cmp_lg_u32 s3, 1
	v_lshl_add_u64 v[2:3], s[20:21], 0, v[130:131]
	s_cbranch_scc1 .LBB0_3673
	s_setprio 1
	s_barrier

.LBB0_3691:
	v_lshlrev_b32_e32 v1, 4, v0
	v_and_b32_e32 v2, 32, v8
	v_bitop3_b32 v2, v1, v2, 48 bitop3:0x6c
	s_add_u32 s49, s8, 0x2a000300
	v_lshrrev_b32_e32 v5, 1, v0
	v_lshrrev_b32_e32 v2, 1, v2
	s_addc_u32 s50, s9, 0
	v_bfe_u32 v3, v0, 2, 26
	v_bfe_u32 v4, v1, 6, 4
	v_and_or_b32 v2, v5, 32, v2
	v_and_b32_e32 v5, 48, v0
	v_lshrrev_b32_e32 v6, 5, v0
	v_lshrrev_b32_e32 v0, 3, v0
	s_mov_b32 s3, 0xfffff0
	s_add_u32 s51, s8, 0x1900000
	v_and_or_b32 v0, v0, s3, v4
	s_addc_u32 s52, s9, 0
	v_and_b32_e32 v6, 4, v6
	v_bfe_u32 v7, v1, 6, 2
	v_mul_u32_u24_e32 v0, 0x300, v0
	s_add_i32 s2, s6, s2
	v_or3_b32 v5, v7, v6, v5
	s_movk_i32 s7, 0xc0
	v_or_b32_e32 v0, v0, v2
	s_ashr_i32 s6, s2, 31
	v_and_or_b32 v3, v3, s7, v5
	v_lshlrev_b32_e32 v128, 1, v0
	v_lshlrev_b32_e32 v0, 1, v2
	v_add_u32_e32 v1, 0x2000, v1
	s_lshr_b32 s6, s6, 26
	v_lshl_or_b32 v130, v3, 9, v0
	v_lshrrev_b32_e32 v3, 7, v1
	v_lshrrev_b32_e32 v1, 6, v1
	s_add_i32 s6, s2, s6
	v_and_or_b32 v1, v1, s7, v5
	s_ashr_i32 s7, s6, 6
	s_and_b32 s6, s6, 0xffc0
	s_sub_i32 s6, s2, s6
	s_bfe_i32 s2, s6, 0x80000
	s_bfe_u32 s2, s2, 0x3000c
	s_add_i32 s13, s6, s2
	s_bfe_i32 s2, s13, 0x80000
	s_and_b32 s13, s13, 0xf8
	s_sub_i32 s6, s6, s13
	s_lshl_b32 s7, s7, 3
	s_sext_i32_i8 s6, s6
	s_ashr_i32 s12, s14, 6
	s_sext_i32_i16 s2, s2
	s_add_i32 s68, s7, s6
	v_and_or_b32 v3, v3, s3, v4
	s_ashr_i32 s3, s14, 8
	s_lshl_b32 s53, s12, 10
	s_lshr_b32 s2, s2, 3
	s_mul_i32 s7, s68, 0x60000
	s_mul_hi_i32 s6, s68, 0x60000
	s_add_u32 s22, s49, s7
	s_addc_u32 s23, s50, s6
	s_bfe_i64 s[6:7], s[2:3], 0x100000
	s_lshl_b64 s[6:7], s[6:7], 17
	s_add_u32 s24, s51, s6
	s_addc_u32 s25, s52, s7
	s_add_i32 s54, s53, 0
	s_add_i32 m0, s54, 0x10000
	v_lshl_or_b32 v134, v1, 9, v0
	global_load_lds_dwordx4 v130, s[24:25]
	s_add_i32 m0, s54, 0x12000
	s_add_u32 s6, s24, 0x1000
	global_load_lds_dwordx4 v134, s[24:25]
	s_addc_u32 s7, s25, 0
	s_add_i32 m0, s54, 0x14000
	v_mul_u32_u24_e32 v3, 0x300, v3
	global_load_lds_dwordx4 v130, s[6:7]
	s_add_i32 m0, s54, 0x16000
	s_add_i32 s55, s54, 0x2000
	v_or_b32_e32 v2, v3, v2
	global_load_lds_dwordx4 v134, s[6:7]
	s_mov_b32 m0, s54
	s_add_u32 s6, s22, 0x30000
	v_lshlrev_b32_e32 v132, 1, v2
	global_load_lds_dwordx4 v128, s[22:23]
	s_mov_b32 m0, s55
	s_addc_u32 s7, s23, 0
	s_add_i32 s56, s54, 0x4000
	global_load_lds_dwordx4 v132, s[22:23]
	s_mov_b32 m0, s56
	s_add_i32 s57, s54, 0x6000
	global_load_lds_dwordx4 v128, s[6:7]
	s_mov_b32 m0, s57
	v_mov_b32_e32 v131, 0
	global_load_lds_dwordx4 v132, s[6:7]
	v_mov_b32_e32 v135, v131
	v_mov_b32_e32 v129, v131
	v_mov_b32_e32 v133, v131
	s_cmp_eq_u32 s3, 1
	s_mov_b32 s58, 0
	v_lshl_add_u64 v[6:7], s[24:25], 0, v[130:131]
	v_lshl_add_u64 v[4:5], s[24:25], 0, v[134:135]
	v_lshl_add_u64 v[0:1], s[22:23], 0, v[128:129]
	s_cselect_b64 s[6:7], -1, 0
	s_setprio 0
	s_cmp_lg_u32 s3, 1
	v_lshl_add_u64 v[2:3], s[22:23], 0, v[132:133]
	s_cbranch_scc1 .LBB0_3693
	s_setprio 1
	s_barrier

.LBB0_4097:
	v_lshlrev_b32_e32 v4, 4, v80
	v_and_b32_e32 v0, 32, v8
	v_bfe_u32 v7, v80, 2, 4
	v_bitop3_b32 v5, v4, v0, 48 bitop3:0x6c
	v_and_b32_e32 v6, 64, v80
	v_lshrrev_b32_e32 v1, 3, v80
	s_mov_b32 s3, 0x1ffff0
	v_or_b32_e32 v0, v5, v6
	v_and_or_b32 v1, v1, s3, v7
	v_add_u32_e32 v9, 0x2000, v4
	s_ashr_i32 s2, s4, 6
	v_lshl_or_b32 v64, v1, 11, v0
	v_lshrrev_b32_e32 v1, 7, v9
	v_and_or_b32 v1, v1, s3, v7
	s_ashr_i32 s3, s4, 8
	s_lshl_b32 s50, s2, 10
	s_add_u32 s51, s30, 0x26000000
	s_addc_u32 s52, s31, 0
	s_add_u32 s12, s30, 0x1f80000
	s_addc_u32 s13, s31, 0
	s_add_i32 s8, s5, s8
	s_ashr_i32 s9, s8, 31
	s_lshl_b64 s[14:15], s[8:9], 19
	s_add_u32 s22, s51, s14
	s_addc_u32 s23, s52, s15
	s_add_i32 s9, s50, 0
	s_add_i32 m0, s9, 0x10000
	v_lshl_or_b32 v66, v1, 11, v0
	global_load_lds_dwordx4 v64, s[12:13]
	s_add_i32 m0, s9, 0x12000
	s_add_u32 s14, s30, 0x1fc0000
	s_addc_u32 s15, s31, 0
	s_add_i32 s53, s9, 0x14000
	global_load_lds_dwordx4 v66, s[12:13]
	s_mov_b32 m0, s53
	s_add_i32 s54, s9, 0x16000
	global_load_lds_dwordx4 v64, s[14:15]
	s_mov_b32 m0, s54
	s_add_i32 s56, s9, 0x2000
	global_load_lds_dwordx4 v66, s[14:15]
	s_mov_b32 m0, s9
	s_add_u32 s14, s22, 0x40000
	global_load_lds_dwordx4 v64, s[22:23]
	s_mov_b32 m0, s56
	s_addc_u32 s15, s23, 0
	s_add_i32 s57, s9, 0x4000
	global_load_lds_dwordx4 v66, s[22:23]
	s_mov_b32 m0, s57
	s_add_i32 s58, s9, 0x6000
	global_load_lds_dwordx4 v64, s[14:15]
	s_mov_b32 m0, s58
	v_mov_b32_e32 v65, 0
	global_load_lds_dwordx4 v66, s[14:15]
	v_mov_b32_e32 v67, v65
	s_cmp_eq_u32 s3, 1
	s_mov_b32 s64, 0
	v_lshl_add_u64 v[0:1], s[22:23], 0, v[64:65]
	s_cselect_b64 s[14:15], -1, 0
	s_setprio 0
	s_cmp_lg_u32 s3, 1
	v_lshl_add_u64 v[2:3], s[22:23], 0, v[66:67]
	s_cbranch_scc1 .LBB0_4099
	s_setprio 1
	s_barrier

.LBB0_4337:
	s_or_b64 exec, exec, s[12:13]
	v_and_b32_e32 v10, 32, v8
	v_bitop3_b32 v10, v2, v10, 48 bitop3:0x6c
	v_and_or_b32 v150, v0, 64, v10
	v_lshlrev_b32_e32 v0, 1, v9
	v_lshrrev_b32_e32 v2, 9, v2
	v_or_b32_e32 v138, v3, v150
	v_and_b32_e32 v0, 24, v0
	v_and_b32_e32 v2, 4, v2
	v_and_b32_e32 v3, 3, v9
	s_ashr_i32 s18, s20, 6
	v_or3_b32 v0, v2, v3, v0
	s_mov_b32 s12, 0x1fffe0
	s_lshl_b32 s29, s18, 10
	v_and_or_b32 v1, v1, s12, v0
	s_add_i32 s49, s29, 0
	v_lshl_or_b32 v128, v1, 11, v150
	s_add_i32 m0, s49, 0x10000
	s_ashr_i32 s21, s20, 8
	v_and_or_b32 v0, v5, s12, v0
	global_load_lds_dwordx4 v128, s[36:37]
	s_add_i32 m0, s49, 0x12000
	v_lshl_or_b32 v130, v0, 11, v150
	s_add_u32 s12, s36, 0x40000
	global_load_lds_dwordx4 v130, s[36:37]
	s_addc_u32 s13, s37, 0
	s_add_i32 m0, s49, 0x14000
	s_add_i32 s50, s49, 0x2000
	global_load_lds_dwordx4 v128, s[12:13]
	s_add_i32 m0, s49, 0x16000
	v_or_b32_e32 v136, v4, v150
	global_load_lds_dwordx4 v130, s[12:13]
	s_mov_b32 m0, s49
	s_add_i32 s51, s49, 0x4000
	global_load_lds_dwordx4 v138, s[30:31]
	s_mov_b32 m0, s50
	v_or_b32_e32 v134, v7, v150
	global_load_lds_dwordx4 v136, s[30:31]
	s_mov_b32 m0, s51
	s_add_i32 s52, s49, 0x6000
	v_or_b32_e32 v140, v6, v150
	global_load_lds_dwordx4 v134, s[30:31]
	s_mov_b32 m0, s52
	v_mov_b32_e32 v133, 0
	global_load_lds_dwordx4 v140, s[30:31]
	v_mov_b32_e32 v129, v133
	v_mov_b32_e32 v131, v133
	v_mov_b32_e32 v139, v133
	v_mov_b32_e32 v137, v133
	s_cmp_eq_u32 s21, 1
	s_mov_b32 s53, 0
	v_lshl_add_u64 v[6:7], s[36:37], 0, v[128:129]
	v_lshl_add_u64 v[4:5], s[36:37], 0, v[130:131]
	v_lshl_add_u64 v[0:1], s[30:31], 0, v[138:139]
	s_cselect_b64 s[12:13], -1, 0
	s_setprio 0
	s_cmp_lg_u32 s21, 1
	v_lshl_add_u64 v[2:3], s[30:31], 0, v[136:137]
	s_cbranch_scc1 .LBB0_4339
	s_setprio 1
	s_barrier

.LBB0_4452:
	v_lshlrev_b32_e32 v1, 4, v0
	v_and_b32_e32 v2, 32, v8
	v_bitop3_b32 v2, v1, v2, 48 bitop3:0x6c
	v_lshrrev_b32_e32 v5, 1, v0
	v_lshrrev_b32_e32 v2, 1, v2
	v_bfe_u32 v3, v0, 2, 26
	v_bfe_u32 v4, v1, 6, 4
	v_and_or_b32 v2, v5, 32, v2
	v_and_b32_e32 v5, 48, v0
	v_lshrrev_b32_e32 v6, 5, v0
	v_lshrrev_b32_e32 v0, 3, v0
	s_mov_b32 s4, 0x1fffff0
	v_and_b32_e32 v6, 4, v6
	v_bfe_u32 v7, v1, 6, 2
	v_and_or_b32 v0, v0, s4, v4
	s_movk_i32 s6, 0x180
	v_or3_b32 v5, v7, v6, v5
	s_movk_i32 s5, 0xc0
	v_mul_lo_u32 v0, v0, s6
	v_and_or_b32 v3, v3, s5, v5
	v_or_b32_e32 v0, v0, v2
	v_lshlrev_b32_e32 v128, 1, v0
	v_mul_u32_u24_e32 v0, 0x180, v3
	v_or_b32_e32 v0, v0, v2
	s_ashr_i32 s14, s16, 6
	v_lshlrev_b32_e32 v130, 1, v0
	v_add_u32_e32 v0, 0x2000, v1
	v_lshrrev_b32_e32 v1, 7, v0
	v_lshrrev_b32_e32 v0, 6, v0
	s_lshl_b32 s45, s14, 10
	v_and_or_b32 v0, v0, s5, v5
	s_add_i32 s46, s45, 0
	v_mul_u32_u24_e32 v0, 0x180, v0
	s_add_i32 m0, s46, 0x10000
	v_or_b32_e32 v0, v0, v2
	s_ashr_i32 s17, s16, 8
	global_load_lds_dwordx4 v130, s[38:39]
	s_add_i32 m0, s46, 0x12000
	v_and_or_b32 v1, v1, s4, v4
	v_lshlrev_b32_e32 v134, 1, v0
	s_add_u32 s4, s38, 0x1800
	global_load_lds_dwordx4 v134, s[38:39]
	s_addc_u32 s5, s39, 0
	s_add_i32 m0, s46, 0x14000
	v_mul_lo_u32 v1, v1, s6
	global_load_lds_dwordx4 v130, s[4:5]
	s_add_i32 m0, s46, 0x16000
	s_add_i32 s47, s46, 0x2000
	v_or_b32_e32 v1, v1, v2
	global_load_lds_dwordx4 v134, s[4:5]
	s_mov_b32 m0, s46
	s_add_u32 s4, s36, 0x18000
	v_lshlrev_b32_e32 v132, 1, v1
	global_load_lds_dwordx4 v128, s[36:37]
	s_mov_b32 m0, s47
	s_addc_u32 s5, s37, 0
	s_add_i32 s49, s46, 0x4000
	global_load_lds_dwordx4 v132, s[36:37]
	s_mov_b32 m0, s49
	s_add_i32 s50, s46, 0x6000
	global_load_lds_dwordx4 v128, s[4:5]
	s_mov_b32 m0, s50
	v_mov_b32_e32 v131, 0
	global_load_lds_dwordx4 v132, s[4:5]
	v_mov_b32_e32 v135, v131
	v_mov_b32_e32 v129, v131
	v_mov_b32_e32 v133, v131
	s_cmp_eq_u32 s17, 1
	v_lshl_add_u64 v[6:7], s[38:39], 0, v[130:131]
	v_lshl_add_u64 v[4:5], s[38:39], 0, v[134:135]
	v_lshl_add_u64 v[0:1], s[36:37], 0, v[128:129]
	s_cselect_b64 s[4:5], -1, 0
	s_setprio 0
	s_cmp_lg_u32 s17, 1
	v_lshl_add_u64 v[2:3], s[36:37], 0, v[132:133]
	s_cbranch_scc1 .LBB0_4454
	s_setprio 1
	s_barrier
